# stack + NSA in-proj epilogue: 13 full vmcnt(0) drains that only waited for store acks removed (table-load waits kept)
# speedup vs baseline: 1.0483x; 1.0002x over previous
.LBB0_184:
	v_cvt_pk_bf16_f32 v146, v146, v147
	v_cvt_pk_bf16_f32 v147, v148, v149
	v_cvt_pk_bf16_f32 v148, v150, v151
	v_lshl_add_u64 v[150:151], v[184:185], 1, s[36:37]
	s_and_b64 vcc, exec, s[14:15]
	v_cvt_pk_bf16_f32 v149, v152, v153
	global_store_dwordx4 v[150:151], v[146:149], off
	s_cbranch_vccnz .LBB0_190
	s_nop 0
	v_mov_b32_e32 v146, v142
	v_mov_b32_e32 v147, v142
	s_nop 1
	v_permlane32_swap_b32_e32 v146, v147
	v_cndmask_b32_e64 v150, v146, v147, s[8:9]
	v_mov_b32_e32 v146, v138
	v_mov_b32_e32 v147, v138
	s_nop 1
	v_permlane32_swap_b32_e32 v146, v147
	v_cndmask_b32_e64 v190, v146, v147, s[8:9]
	v_mov_b32_e32 v146, v143
	v_mov_b32_e32 v147, v143
	s_nop 1
	v_permlane32_swap_b32_e32 v146, v147
	v_cndmask_b32_e64 v151, v146, v147, s[8:9]
	v_mov_b32_e32 v146, v139
	v_mov_b32_e32 v147, v139
	s_nop 1
	v_permlane32_swap_b32_e32 v146, v147
	v_cndmask_b32_e64 v191, v146, v147, s[8:9]
	v_mov_b32_e32 v146, v144
	v_mov_b32_e32 v147, v144
	s_nop 1
	v_permlane32_swap_b32_e32 v146, v147
	v_cndmask_b32_e64 v152, v146, v147, s[8:9]
	v_mov_b32_e32 v146, v140
	v_mov_b32_e32 v147, v140
	s_nop 1
	v_permlane32_swap_b32_e32 v146, v147
	v_cndmask_b32_e64 v186, v146, v147, s[8:9]
	v_mov_b32_e32 v146, v145
	v_mov_b32_e32 v147, v145
	s_nop 1
	v_permlane32_swap_b32_e32 v146, v147
	v_cndmask_b32_e64 v153, v146, v147, s[8:9]
	v_mov_b32_e32 v146, v141
	v_mov_b32_e32 v147, v141
	s_nop 1
	v_permlane32_swap_b32_e32 v146, v147
	v_cndmask_b32_e64 v187, v146, v147, s[8:9]
	v_pk_mul_f32 v[146:147], v[144:145], v[96:97]
	v_pk_mul_f32 v[148:149], v[142:143], v[94:95]
	v_pk_mul_f32 v[184:185], v[104:105], v[152:153]
	v_pk_mul_f32 v[188:189], v[102:103], v[150:151]
	v_pk_mul_f32 v[150:151], v[140:141], v[92:93]
	v_pk_mul_f32 v[152:153], v[138:139], v[90:91]
	v_pk_mul_f32 v[186:187], v[100:101], v[186:187]
	v_pk_mul_f32 v[190:191], v[98:99], v[190:191]
	s_and_saveexec_b64 s[40:41], s[10:11]
	s_xor_b64 s[40:41], exec, s[40:41]
	v_pk_add_f32 v[144:145], v[146:147], v[184:185]
	v_pk_add_f32 v[142:143], v[148:149], v[188:189]
	v_pk_add_f32 v[140:141], v[150:151], v[186:187]
	v_pk_add_f32 v[138:139], v[152:153], v[190:191]
	s_andn2_saveexec_b64 s[40:41], s[40:41]
	v_sub_f32_e32 v145, v147, v185
	v_sub_f32_e32 v144, v146, v184
	v_sub_f32_e32 v143, v149, v189
	v_sub_f32_e32 v142, v148, v188
	v_sub_f32_e32 v141, v151, v187
	v_sub_f32_e32 v140, v150, v186
	v_sub_f32_e32 v139, v153, v191
	v_sub_f32_e32 v138, v152, v190
	s_or_b64 exec, exec, s[40:41]

.LBB0_194:
	v_cvt_pk_bf16_f32 v142, v142, v143
	v_cvt_pk_bf16_f32 v143, v144, v145
	v_cvt_pk_bf16_f32 v144, v138, v139
	v_lshl_add_u64 v[138:139], v[148:149], 1, s[36:37]
	s_and_b64 vcc, exec, s[14:15]
	v_bitop3_b32 v192, v200, s59, 16 bitop3:0xc8
	v_cvt_pk_bf16_f32 v145, v140, v141
	global_store_dwordx4 v[138:139], v[142:145], off
	s_cbranch_vccnz .LBB0_196
	v_lshlrev_b32_e32 v162, 6, v192
	v_lshl_add_u64 v[102:103], v[166:167], 0, v[162:163]
	v_lshl_add_u64 v[94:95], v[168:169], 0, v[162:163]
	global_load_dwordx4 v[90:93], v[94:95], off offset:16
	s_nop 0
	global_load_dwordx4 v[94:97], v[94:95], off
	s_nop 0
	global_load_dwordx4 v[98:101], v[102:103], off offset:16
	s_nop 0
	global_load_dwordx4 v[102:105], v[102:103], off

.LBB0_210:
	v_cvt_pk_bf16_f32 v134, v134, v135
	v_cvt_pk_bf16_f32 v135, v136, v137
	v_cvt_pk_bf16_f32 v136, v130, v131
	v_lshl_add_u64 v[130:131], v[138:139], 1, s[36:37]
	s_and_b64 vcc, exec, s[14:15]
	v_bitop3_b32 v184, v200, s60, 32 bitop3:0xc8
	v_cvt_pk_bf16_f32 v137, v132, v133
	global_store_dwordx4 v[130:131], v[134:137], off
	s_cbranch_vccnz .LBB0_212
	v_lshlrev_b32_e32 v162, 6, v184
	v_lshl_add_u64 v[102:103], v[166:167], 0, v[162:163]
	v_lshl_add_u64 v[94:95], v[168:169], 0, v[162:163]
	global_load_dwordx4 v[90:93], v[94:95], off offset:16
	s_nop 0
	global_load_dwordx4 v[94:97], v[94:95], off
	s_nop 0
	global_load_dwordx4 v[98:101], v[102:103], off offset:16
	s_nop 0
	global_load_dwordx4 v[102:105], v[102:103], off

.LBB0_226:
	v_cvt_pk_bf16_f32 v126, v126, v127
	v_cvt_pk_bf16_f32 v127, v128, v129
	v_cvt_pk_bf16_f32 v128, v122, v123
	v_lshl_add_u64 v[122:123], v[130:131], 1, s[36:37]
	s_and_b64 vcc, exec, s[14:15]
	v_bitop3_b32 v148, v200, s61, 48 bitop3:0xc8
	v_cvt_pk_bf16_f32 v129, v124, v125
	global_store_dwordx4 v[122:123], v[126:129], off
	s_cbranch_vccnz .LBB0_228
	v_lshlrev_b32_e32 v162, 6, v148
	v_lshl_add_u64 v[102:103], v[166:167], 0, v[162:163]
	v_lshl_add_u64 v[94:95], v[168:169], 0, v[162:163]
	global_load_dwordx4 v[90:93], v[94:95], off offset:16
	s_nop 0
	global_load_dwordx4 v[94:97], v[94:95], off
	s_nop 0
	global_load_dwordx4 v[98:101], v[102:103], off offset:16
	s_nop 0
	global_load_dwordx4 v[102:105], v[102:103], off

.LBB0_242:
	v_add_u32_e32 v138, 0x80, v200
	v_cvt_pk_bf16_f32 v118, v118, v119
	v_cvt_pk_bf16_f32 v119, v120, v121
	v_cvt_pk_bf16_f32 v120, v114, v115
	v_lshl_add_u64 v[114:115], v[122:123], 1, s[36:37]
	s_and_b64 vcc, exec, s[14:15]
	v_and_b32_e32 v139, 0xfcf, v138
	v_cvt_pk_bf16_f32 v121, v116, v117
	global_store_dwordx4 v[114:115], v[118:121], off
	s_cbranch_vccnz .LBB0_244
	v_lshlrev_b32_e32 v162, 6, v139
	v_lshl_add_u64 v[102:103], v[166:167], 0, v[162:163]
	v_lshl_add_u64 v[94:95], v[168:169], 0, v[162:163]
	global_load_dwordx4 v[90:93], v[94:95], off offset:16
	s_nop 0
	global_load_dwordx4 v[94:97], v[94:95], off
	s_nop 0
	global_load_dwordx4 v[98:101], v[102:103], off offset:16
	s_nop 0
	global_load_dwordx4 v[102:105], v[102:103], off

.LBB0_258:
	v_add_u32_e32 v131, 0x90, v200
	v_cvt_pk_bf16_f32 v110, v110, v111
	v_cvt_pk_bf16_f32 v111, v112, v113
	v_cvt_pk_bf16_f32 v112, v106, v107
	v_lshl_add_u64 v[106:107], v[114:115], 1, s[36:37]
	s_and_b64 vcc, exec, s[14:15]
	v_and_b32_e32 v130, 0xfdf, v131
	v_cvt_pk_bf16_f32 v113, v108, v109
	global_store_dwordx4 v[106:107], v[110:113], off
	s_cbranch_vccnz .LBB0_260
	v_lshlrev_b32_e32 v162, 6, v130
	v_lshl_add_u64 v[102:103], v[166:167], 0, v[162:163]
	v_lshl_add_u64 v[94:95], v[168:169], 0, v[162:163]
	global_load_dwordx4 v[90:93], v[94:95], off offset:16
	s_nop 0
	global_load_dwordx4 v[94:97], v[94:95], off
	s_nop 0
	global_load_dwordx4 v[98:101], v[102:103], off offset:16
	s_nop 0
	global_load_dwordx4 v[102:105], v[102:103], off

.LBB0_312:
	s_nop 0
	v_mov_b32_e32 v138, v134
	v_mov_b32_e32 v139, v134
	s_nop 1
	v_permlane32_swap_b32_e32 v138, v139
	v_cndmask_b32_e64 v142, v138, v139, s[8:9]
	v_mov_b32_e32 v138, v130
	v_mov_b32_e32 v139, v130
	s_nop 1
	v_permlane32_swap_b32_e32 v138, v139
	v_cndmask_b32_e64 v184, v138, v139, s[8:9]
	v_mov_b32_e32 v138, v135
	v_mov_b32_e32 v139, v135
	s_nop 1
	v_permlane32_swap_b32_e32 v138, v139
	v_cndmask_b32_e64 v143, v138, v139, s[8:9]
	v_mov_b32_e32 v138, v131
	v_mov_b32_e32 v139, v131
	s_nop 1
	v_permlane32_swap_b32_e32 v138, v139
	v_cndmask_b32_e64 v185, v138, v139, s[8:9]
	v_mov_b32_e32 v138, v136
	v_mov_b32_e32 v139, v136
	s_nop 1
	v_permlane32_swap_b32_e32 v138, v139
	v_cndmask_b32_e64 v144, v138, v139, s[8:9]
	v_mov_b32_e32 v138, v132
	v_mov_b32_e32 v139, v132
	s_nop 1
	v_permlane32_swap_b32_e32 v138, v139
	v_cndmask_b32_e64 v152, v138, v139, s[8:9]
	v_mov_b32_e32 v138, v137
	v_mov_b32_e32 v139, v137
	s_nop 1
	v_permlane32_swap_b32_e32 v138, v139
	v_cndmask_b32_e64 v145, v138, v139, s[8:9]
	v_mov_b32_e32 v138, v133
	v_mov_b32_e32 v139, v133
	s_nop 1
	v_permlane32_swap_b32_e32 v138, v139
	v_cndmask_b32_e64 v153, v138, v139, s[8:9]
	v_pk_mul_f32 v[138:139], v[136:137], v[96:97]
	v_pk_mul_f32 v[140:141], v[134:135], v[94:95]
	v_pk_mul_f32 v[150:151], v[104:105], v[144:145]
	v_pk_mul_f32 v[182:183], v[102:103], v[142:143]
	v_pk_mul_f32 v[142:143], v[132:133], v[92:93]
	v_pk_mul_f32 v[144:145], v[130:131], v[90:91]
	v_pk_mul_f32 v[152:153], v[100:101], v[152:153]
	v_pk_mul_f32 v[184:185], v[98:99], v[184:185]
	s_and_saveexec_b64 s[40:41], s[10:11]
	s_xor_b64 s[40:41], exec, s[40:41]
	v_pk_add_f32 v[136:137], v[138:139], v[150:151]
	v_pk_add_f32 v[134:135], v[140:141], v[182:183]
	v_pk_add_f32 v[132:133], v[142:143], v[152:153]
	v_pk_add_f32 v[130:131], v[144:145], v[184:185]
	s_andn2_saveexec_b64 s[40:41], s[40:41]
	v_sub_f32_e32 v137, v139, v151
	v_sub_f32_e32 v136, v138, v150
	v_sub_f32_e32 v135, v141, v183
	v_sub_f32_e32 v134, v140, v182
	v_sub_f32_e32 v133, v143, v153
	v_sub_f32_e32 v132, v142, v152
	v_sub_f32_e32 v131, v145, v185
	v_sub_f32_e32 v130, v144, v184
	s_or_b64 exec, exec, s[40:41]
	s_and_b64 vcc, exec, s[16:17]
	s_mov_b64 s[40:41], -1
	s_cbranch_vccnz .LBB0_208

.LBB0_318:
	s_nop 0
	v_mov_b32_e32 v130, v126
	v_mov_b32_e32 v131, v126
	s_nop 1
	v_permlane32_swap_b32_e32 v130, v131
	v_cndmask_b32_e64 v134, v130, v131, s[8:9]
	v_mov_b32_e32 v130, v122
	v_mov_b32_e32 v131, v122
	s_nop 1
	v_permlane32_swap_b32_e32 v130, v131
	v_cndmask_b32_e64 v148, v130, v131, s[8:9]
	v_mov_b32_e32 v130, v127
	v_mov_b32_e32 v131, v127
	s_nop 1
	v_permlane32_swap_b32_e32 v130, v131
	v_cndmask_b32_e64 v135, v130, v131, s[8:9]
	v_mov_b32_e32 v130, v123
	v_mov_b32_e32 v131, v123
	s_nop 1
	v_permlane32_swap_b32_e32 v130, v131
	v_cndmask_b32_e64 v149, v130, v131, s[8:9]
	v_mov_b32_e32 v130, v128
	v_mov_b32_e32 v131, v128
	s_nop 1
	v_permlane32_swap_b32_e32 v130, v131
	v_cndmask_b32_e64 v136, v130, v131, s[8:9]
	v_mov_b32_e32 v130, v124
	v_mov_b32_e32 v131, v124
	s_nop 1
	v_permlane32_swap_b32_e32 v130, v131
	v_cndmask_b32_e64 v142, v130, v131, s[8:9]
	v_mov_b32_e32 v130, v129
	v_mov_b32_e32 v131, v129
	s_nop 1
	v_permlane32_swap_b32_e32 v130, v131
	v_cndmask_b32_e64 v137, v130, v131, s[8:9]
	v_mov_b32_e32 v130, v125
	v_mov_b32_e32 v131, v125
	s_nop 1
	v_permlane32_swap_b32_e32 v130, v131
	v_cndmask_b32_e64 v143, v130, v131, s[8:9]
	v_pk_mul_f32 v[130:131], v[128:129], v[96:97]
	v_pk_mul_f32 v[132:133], v[126:127], v[94:95]
	v_pk_mul_f32 v[140:141], v[104:105], v[136:137]
	v_pk_mul_f32 v[144:145], v[102:103], v[134:135]
	v_pk_mul_f32 v[134:135], v[124:125], v[92:93]
	v_pk_mul_f32 v[136:137], v[122:123], v[90:91]
	v_pk_mul_f32 v[142:143], v[100:101], v[142:143]
	v_pk_mul_f32 v[148:149], v[98:99], v[148:149]
	s_and_saveexec_b64 s[40:41], s[10:11]
	s_xor_b64 s[40:41], exec, s[40:41]
	v_pk_add_f32 v[128:129], v[130:131], v[140:141]
	v_pk_add_f32 v[126:127], v[132:133], v[144:145]
	v_pk_add_f32 v[124:125], v[134:135], v[142:143]
	v_pk_add_f32 v[122:123], v[136:137], v[148:149]
	s_andn2_saveexec_b64 s[40:41], s[40:41]
	v_sub_f32_e32 v129, v131, v141
	v_sub_f32_e32 v128, v130, v140
	v_sub_f32_e32 v127, v133, v145
	v_sub_f32_e32 v126, v132, v144
	v_sub_f32_e32 v125, v135, v143
	v_sub_f32_e32 v124, v134, v142
	v_sub_f32_e32 v123, v137, v149
	v_sub_f32_e32 v122, v136, v148
	s_or_b64 exec, exec, s[40:41]
	s_and_b64 vcc, exec, s[16:17]
	s_mov_b64 s[40:41], -1
	s_cbranch_vccnz .LBB0_224

.LBB0_324:
	s_nop 0
	v_mov_b32_e32 v122, v118
	v_mov_b32_e32 v123, v118
	s_nop 1
	v_permlane32_swap_b32_e32 v122, v123
	v_cndmask_b32_e64 v126, v122, v123, s[8:9]
	v_mov_b32_e32 v122, v114
	v_mov_b32_e32 v123, v114
	s_nop 1
	v_permlane32_swap_b32_e32 v122, v123
	v_cndmask_b32_e64 v138, v122, v123, s[8:9]
	v_mov_b32_e32 v122, v119
	v_mov_b32_e32 v123, v119
	s_nop 1
	v_permlane32_swap_b32_e32 v122, v123
	v_cndmask_b32_e64 v127, v122, v123, s[8:9]
	v_mov_b32_e32 v122, v115
	v_mov_b32_e32 v123, v115
	s_nop 1
	v_permlane32_swap_b32_e32 v122, v123
	v_cndmask_b32_e64 v139, v122, v123, s[8:9]
	v_mov_b32_e32 v122, v120
	v_mov_b32_e32 v123, v120
	s_nop 1
	v_permlane32_swap_b32_e32 v122, v123
	v_cndmask_b32_e64 v128, v122, v123, s[8:9]
	v_mov_b32_e32 v122, v116
	v_mov_b32_e32 v123, v116
	s_nop 1
	v_permlane32_swap_b32_e32 v122, v123
	v_cndmask_b32_e64 v134, v122, v123, s[8:9]
	v_mov_b32_e32 v122, v121
	v_mov_b32_e32 v123, v121
	s_nop 1
	v_permlane32_swap_b32_e32 v122, v123
	v_cndmask_b32_e64 v129, v122, v123, s[8:9]
	v_mov_b32_e32 v122, v117
	v_mov_b32_e32 v123, v117
	s_nop 1
	v_permlane32_swap_b32_e32 v122, v123
	v_cndmask_b32_e64 v135, v122, v123, s[8:9]
	v_pk_mul_f32 v[122:123], v[120:121], v[96:97]
	v_pk_mul_f32 v[124:125], v[118:119], v[94:95]
	v_pk_mul_f32 v[132:133], v[104:105], v[128:129]
	v_pk_mul_f32 v[136:137], v[102:103], v[126:127]
	v_pk_mul_f32 v[126:127], v[116:117], v[92:93]
	v_pk_mul_f32 v[128:129], v[114:115], v[90:91]
	v_pk_mul_f32 v[134:135], v[100:101], v[134:135]
	v_pk_mul_f32 v[138:139], v[98:99], v[138:139]
	s_and_saveexec_b64 s[40:41], s[10:11]
	s_xor_b64 s[40:41], exec, s[40:41]
	v_pk_add_f32 v[120:121], v[122:123], v[132:133]
	v_pk_add_f32 v[118:119], v[124:125], v[136:137]
	v_pk_add_f32 v[116:117], v[126:127], v[134:135]
	v_pk_add_f32 v[114:115], v[128:129], v[138:139]
	s_andn2_saveexec_b64 s[40:41], s[40:41]
	v_sub_f32_e32 v121, v123, v133
	v_sub_f32_e32 v120, v122, v132
	v_sub_f32_e32 v119, v125, v137
	v_sub_f32_e32 v118, v124, v136
	v_sub_f32_e32 v117, v127, v135
	v_sub_f32_e32 v116, v126, v134
	v_sub_f32_e32 v115, v129, v139
	v_sub_f32_e32 v114, v128, v138
	s_or_b64 exec, exec, s[40:41]
	s_and_b64 vcc, exec, s[16:17]
	s_mov_b64 s[40:41], -1
	s_cbranch_vccnz .LBB0_240

.LBB0_330:
	s_nop 0
	v_mov_b32_e32 v114, v110
	v_mov_b32_e32 v115, v110
	s_nop 1
	v_permlane32_swap_b32_e32 v114, v115
	v_cndmask_b32_e64 v118, v114, v115, s[8:9]
	v_mov_b32_e32 v114, v106
	v_mov_b32_e32 v115, v106
	s_nop 1
	v_permlane32_swap_b32_e32 v114, v115
	v_cndmask_b32_e64 v130, v114, v115, s[8:9]
	v_mov_b32_e32 v114, v111
	v_mov_b32_e32 v115, v111
	s_nop 1
	v_permlane32_swap_b32_e32 v114, v115
	v_cndmask_b32_e64 v119, v114, v115, s[8:9]
	v_mov_b32_e32 v114, v107
	v_mov_b32_e32 v115, v107
	s_nop 1
	v_permlane32_swap_b32_e32 v114, v115
	v_cndmask_b32_e64 v131, v114, v115, s[8:9]
	v_mov_b32_e32 v114, v112
	v_mov_b32_e32 v115, v112
	s_nop 1
	v_permlane32_swap_b32_e32 v114, v115
	v_cndmask_b32_e64 v120, v114, v115, s[8:9]
	v_mov_b32_e32 v114, v108
	v_mov_b32_e32 v115, v108
	s_nop 1
	v_permlane32_swap_b32_e32 v114, v115
	v_cndmask_b32_e64 v126, v114, v115, s[8:9]
	v_mov_b32_e32 v114, v113
	v_mov_b32_e32 v115, v113
	s_nop 1
	v_permlane32_swap_b32_e32 v114, v115
	v_cndmask_b32_e64 v121, v114, v115, s[8:9]
	v_mov_b32_e32 v114, v109
	v_mov_b32_e32 v115, v109
	s_nop 1
	v_permlane32_swap_b32_e32 v114, v115
	v_cndmask_b32_e64 v127, v114, v115, s[8:9]
	v_pk_mul_f32 v[114:115], v[112:113], v[96:97]
	v_pk_mul_f32 v[116:117], v[110:111], v[94:95]
	v_pk_mul_f32 v[124:125], v[104:105], v[120:121]
	v_pk_mul_f32 v[128:129], v[102:103], v[118:119]
	v_pk_mul_f32 v[118:119], v[108:109], v[92:93]
	v_pk_mul_f32 v[120:121], v[106:107], v[90:91]
	v_pk_mul_f32 v[126:127], v[100:101], v[126:127]
	v_pk_mul_f32 v[130:131], v[98:99], v[130:131]
	s_and_saveexec_b64 s[40:41], s[10:11]
	s_xor_b64 s[40:41], exec, s[40:41]
	v_pk_add_f32 v[112:113], v[114:115], v[124:125]
	v_pk_add_f32 v[110:111], v[116:117], v[128:129]
	v_pk_add_f32 v[108:109], v[118:119], v[126:127]
	v_pk_add_f32 v[106:107], v[120:121], v[130:131]
	s_andn2_saveexec_b64 s[40:41], s[40:41]
	v_sub_f32_e32 v113, v115, v125
	v_sub_f32_e32 v112, v114, v124
	v_sub_f32_e32 v111, v117, v129
	v_sub_f32_e32 v110, v116, v128
	v_sub_f32_e32 v109, v119, v127
	v_sub_f32_e32 v108, v118, v126
	v_sub_f32_e32 v107, v121, v131
	v_sub_f32_e32 v106, v120, v130
	s_or_b64 exec, exec, s[40:41]
	s_and_b64 vcc, exec, s[16:17]
	s_mov_b64 s[40:41], -1
	s_cbranch_vccnz .LBB0_256

.LBB0_336:
	s_nop 0
	v_mov_b32_e32 v106, v86
	v_mov_b32_e32 v107, v86
	s_nop 1
	v_permlane32_swap_b32_e32 v106, v107
	v_cndmask_b32_e64 v110, v106, v107, s[8:9]
	v_mov_b32_e32 v106, v82
	v_mov_b32_e32 v107, v82
	s_nop 1
	v_permlane32_swap_b32_e32 v106, v107
	v_cndmask_b32_e64 v122, v106, v107, s[8:9]
	v_mov_b32_e32 v106, v87
	v_mov_b32_e32 v107, v87
	s_nop 1
	v_permlane32_swap_b32_e32 v106, v107
	v_cndmask_b32_e64 v111, v106, v107, s[8:9]
	v_mov_b32_e32 v106, v83
	v_mov_b32_e32 v107, v83
	s_nop 1
	v_permlane32_swap_b32_e32 v106, v107
	v_cndmask_b32_e64 v123, v106, v107, s[8:9]
	v_mov_b32_e32 v106, v88
	v_mov_b32_e32 v107, v88
	s_nop 1
	v_permlane32_swap_b32_e32 v106, v107
	v_cndmask_b32_e64 v112, v106, v107, s[8:9]
	v_mov_b32_e32 v106, v84
	v_mov_b32_e32 v107, v84
	s_nop 1
	v_permlane32_swap_b32_e32 v106, v107
	v_cndmask_b32_e64 v118, v106, v107, s[8:9]
	v_mov_b32_e32 v106, v89
	v_mov_b32_e32 v107, v89
	s_nop 1
	v_permlane32_swap_b32_e32 v106, v107
	v_cndmask_b32_e64 v113, v106, v107, s[8:9]
	v_mov_b32_e32 v106, v85
	v_mov_b32_e32 v107, v85
	s_nop 1
	v_permlane32_swap_b32_e32 v106, v107
	v_cndmask_b32_e64 v119, v106, v107, s[8:9]
	v_pk_mul_f32 v[106:107], v[88:89], v[96:97]
	v_pk_mul_f32 v[108:109], v[86:87], v[94:95]
	v_pk_mul_f32 v[116:117], v[104:105], v[112:113]
	v_pk_mul_f32 v[120:121], v[102:103], v[110:111]
	v_pk_mul_f32 v[110:111], v[84:85], v[92:93]
	v_pk_mul_f32 v[112:113], v[82:83], v[90:91]
	v_pk_mul_f32 v[118:119], v[100:101], v[118:119]
	v_pk_mul_f32 v[122:123], v[98:99], v[122:123]
	s_and_saveexec_b64 s[40:41], s[10:11]
	s_xor_b64 s[40:41], exec, s[40:41]
	v_pk_add_f32 v[88:89], v[106:107], v[116:117]
	v_pk_add_f32 v[86:87], v[108:109], v[120:121]
	v_pk_add_f32 v[84:85], v[110:111], v[118:119]
	v_pk_add_f32 v[82:83], v[112:113], v[122:123]
	s_andn2_saveexec_b64 s[40:41], s[40:41]
	v_sub_f32_e32 v89, v107, v117
	v_sub_f32_e32 v88, v106, v116
	v_sub_f32_e32 v87, v109, v121
	v_sub_f32_e32 v86, v108, v120
	v_sub_f32_e32 v85, v111, v119
	v_sub_f32_e32 v84, v110, v118
	v_sub_f32_e32 v83, v113, v123
	v_sub_f32_e32 v82, v112, v122
	s_or_b64 exec, exec, s[40:41]
	s_and_b64 vcc, exec, s[16:17]
	s_mov_b64 s[40:41], -1
	s_cbranch_vccnz .LBB0_272

.LBB0_342:
	s_nop 0
	v_mov_b32_e32 v82, v78
	v_mov_b32_e32 v83, v78
	s_nop 1
	v_permlane32_swap_b32_e32 v82, v83
	v_cndmask_b32_e64 v86, v82, v83, s[8:9]
	v_mov_b32_e32 v82, v74
	v_mov_b32_e32 v83, v74
	s_nop 1
	v_permlane32_swap_b32_e32 v82, v83
	v_cndmask_b32_e64 v114, v82, v83, s[8:9]
	v_mov_b32_e32 v82, v79
	v_mov_b32_e32 v83, v79
	s_nop 1
	v_permlane32_swap_b32_e32 v82, v83
	v_cndmask_b32_e64 v87, v82, v83, s[8:9]
	v_mov_b32_e32 v82, v75
	v_mov_b32_e32 v83, v75
	s_nop 1
	v_permlane32_swap_b32_e32 v82, v83
	v_cndmask_b32_e64 v115, v82, v83, s[8:9]
	v_mov_b32_e32 v82, v80
	v_mov_b32_e32 v83, v80
	s_nop 1
	v_permlane32_swap_b32_e32 v82, v83
	v_cndmask_b32_e64 v88, v82, v83, s[8:9]
	v_mov_b32_e32 v82, v76
	v_mov_b32_e32 v83, v76
	s_nop 1
	v_permlane32_swap_b32_e32 v82, v83
	v_cndmask_b32_e64 v110, v82, v83, s[8:9]
	v_mov_b32_e32 v82, v81
	v_mov_b32_e32 v83, v81
	s_nop 1
	v_permlane32_swap_b32_e32 v82, v83
	v_cndmask_b32_e64 v89, v82, v83, s[8:9]
	v_mov_b32_e32 v82, v77
	v_mov_b32_e32 v83, v77
	s_nop 1
	v_permlane32_swap_b32_e32 v82, v83
	v_cndmask_b32_e64 v111, v82, v83, s[8:9]
	v_pk_mul_f32 v[82:83], v[80:81], v[96:97]
	v_pk_mul_f32 v[84:85], v[78:79], v[94:95]
	v_pk_mul_f32 v[108:109], v[104:105], v[88:89]
	v_pk_mul_f32 v[112:113], v[102:103], v[86:87]
	v_pk_mul_f32 v[86:87], v[76:77], v[92:93]
	v_pk_mul_f32 v[88:89], v[74:75], v[90:91]
	v_pk_mul_f32 v[110:111], v[100:101], v[110:111]
	v_pk_mul_f32 v[114:115], v[98:99], v[114:115]
	s_and_saveexec_b64 s[40:41], s[10:11]
	s_xor_b64 s[40:41], exec, s[40:41]
	v_pk_add_f32 v[80:81], v[82:83], v[108:109]
	v_pk_add_f32 v[78:79], v[84:85], v[112:113]
	v_pk_add_f32 v[76:77], v[86:87], v[110:111]
	v_pk_add_f32 v[74:75], v[88:89], v[114:115]
	s_andn2_saveexec_b64 s[40:41], s[40:41]
	v_sub_f32_e32 v81, v83, v109
	v_sub_f32_e32 v80, v82, v108
	v_sub_f32_e32 v79, v85, v113
	v_sub_f32_e32 v78, v84, v112
	v_sub_f32_e32 v77, v87, v111
	v_sub_f32_e32 v76, v86, v110
	v_sub_f32_e32 v75, v89, v115
	v_sub_f32_e32 v74, v88, v114
	s_or_b64 exec, exec, s[40:41]
	s_and_b64 vcc, exec, s[16:17]
	s_mov_b64 s[40:41], -1
	s_cbranch_vccnz .LBB0_288

.LBB0_348:
	s_nop 0
	v_mov_b32_e32 v74, v62
	v_mov_b32_e32 v75, v62
	s_nop 1
	v_permlane32_swap_b32_e32 v74, v75
	v_cndmask_b32_e64 v78, v74, v75, s[8:9]
	v_mov_b32_e32 v74, v58
	v_mov_b32_e32 v75, v58
	s_nop 1
	v_permlane32_swap_b32_e32 v74, v75
	v_cndmask_b32_e64 v108, v74, v75, s[8:9]
	v_mov_b32_e32 v74, v63
	v_mov_b32_e32 v75, v63
	s_nop 1
	v_permlane32_swap_b32_e32 v74, v75
	v_cndmask_b32_e64 v79, v74, v75, s[8:9]
	v_mov_b32_e32 v74, v59
	v_mov_b32_e32 v75, v59
	s_nop 1
	v_permlane32_swap_b32_e32 v74, v75
	v_cndmask_b32_e64 v109, v74, v75, s[8:9]
	v_mov_b32_e32 v74, v64
	v_mov_b32_e32 v75, v64
	s_nop 1
	v_permlane32_swap_b32_e32 v74, v75
	v_cndmask_b32_e64 v80, v74, v75, s[8:9]
	v_mov_b32_e32 v74, v60
	v_mov_b32_e32 v75, v60
	s_nop 1
	v_permlane32_swap_b32_e32 v74, v75
	v_cndmask_b32_e64 v86, v74, v75, s[8:9]
	v_mov_b32_e32 v74, v65
	v_mov_b32_e32 v75, v65
	s_nop 1
	v_permlane32_swap_b32_e32 v74, v75
	v_cndmask_b32_e64 v81, v74, v75, s[8:9]
	v_mov_b32_e32 v74, v61
	v_mov_b32_e32 v75, v61
	s_nop 1
	v_permlane32_swap_b32_e32 v74, v75
	v_cndmask_b32_e64 v87, v74, v75, s[8:9]
	v_pk_mul_f32 v[74:75], v[64:65], v[96:97]
	v_pk_mul_f32 v[76:77], v[62:63], v[94:95]
	v_pk_mul_f32 v[84:85], v[104:105], v[80:81]
	v_pk_mul_f32 v[88:89], v[102:103], v[78:79]
	v_pk_mul_f32 v[78:79], v[60:61], v[92:93]
	v_pk_mul_f32 v[80:81], v[58:59], v[90:91]
	v_pk_mul_f32 v[86:87], v[100:101], v[86:87]
	v_pk_mul_f32 v[90:91], v[98:99], v[108:109]
	s_and_saveexec_b64 s[14:15], s[10:11]
	s_xor_b64 s[14:15], exec, s[14:15]
	v_pk_add_f32 v[64:65], v[74:75], v[84:85]
	v_pk_add_f32 v[62:63], v[76:77], v[88:89]
	v_pk_add_f32 v[60:61], v[78:79], v[86:87]
	v_pk_add_f32 v[58:59], v[80:81], v[90:91]
	s_andn2_saveexec_b64 s[14:15], s[14:15]
	v_sub_f32_e32 v65, v75, v85
	v_sub_f32_e32 v64, v74, v84
	v_sub_f32_e32 v63, v77, v89
	v_sub_f32_e32 v62, v76, v88
	v_sub_f32_e32 v61, v79, v87
	v_sub_f32_e32 v60, v78, v86
	v_sub_f32_e32 v59, v81, v91
	v_sub_f32_e32 v58, v80, v90
	s_or_b64 exec, exec, s[14:15]
	s_and_b64 vcc, exec, s[16:17]
	s_mov_b64 s[14:15], -1
	s_cbranch_vccnz .LBB0_304
